# v60 + conv step: LDS-read waits merged pairwise (7 fewer s_waitcnt per step)
# speedup vs baseline: 1.0088x; 1.0016x over previous
; __device__ __forceinline__ void ph_conv2(const Params& p, int l, LAS unsigned char* lds, const int wvid) {
;     ...
;             for (int i = 0; i < 38; ++i) x[i] = G[(tl + i) * 256 + c];
; #pragma unroll
;             for (int o = 0; o < 8; ++o) { float acc = cb;
; #pragma unroll
;                 for (int w = 0; w < 31; ++w) acc += wv[w] * x[o + w];
.LBB0_456:
	ds_read2st64_b32 v[40:41], v0 offset1:4
	ds_read2st64_b32 v[38:39], v0 offset0:8 offset1:12
	ds_read2st64_b32 v[36:37], v0 offset0:16 offset1:20
	ds_read2st64_b32 v[34:35], v0 offset0:24 offset1:28
	ds_read2st64_b32 v[32:33], v0 offset0:32 offset1:36
	ds_read2st64_b32 v[30:31], v0 offset0:40 offset1:44
	ds_read2st64_b32 v[28:29], v0 offset0:48 offset1:52
	ds_read2st64_b32 v[26:27], v0 offset0:56 offset1:60
	ds_read2st64_b32 v[24:25], v0 offset0:64 offset1:68
	ds_read2st64_b32 v[22:23], v0 offset0:72 offset1:76
	ds_read2st64_b32 v[20:21], v0 offset0:80 offset1:84
	ds_read2st64_b32 v[18:19], v0 offset0:88 offset1:92
	ds_read2st64_b32 v[16:17], v0 offset0:96 offset1:100
	ds_read2st64_b32 v[14:15], v0 offset0:104 offset1:108
	ds_read2st64_b32 v[12:13], v0 offset0:112 offset1:116
	ds_read2st64_b32 v[10:11], v0 offset0:120 offset1:124
	ds_read2st64_b32 v[8:9], v0 offset0:128 offset1:132
	ds_read2st64_b32 v[6:7], v0 offset0:136 offset1:140
	ds_read2st64_b32 v[4:5], v0 offset0:144 offset1:148
	s_waitcnt lgkmcnt(15)
	v_fma_f32 v120, v60, v40, v55
	v_fmac_f32_e32 v120, v61, v41
	s_waitcnt lgkmcnt(15)
	v_fmac_f32_e32 v120, v62, v38
	v_fmac_f32_e32 v120, v63, v39
	s_waitcnt lgkmcnt(15)
	v_fmac_f32_e32 v120, v64, v36
	v_fmac_f32_e32 v120, v65, v37
	s_waitcnt lgkmcnt(15)
	v_fmac_f32_e32 v120, v66, v34
	v_fmac_f32_e32 v120, v67, v35
	s_waitcnt lgkmcnt(13)
	v_fmac_f32_e32 v120, v68, v32
	v_fmac_f32_e32 v120, v69, v33
	v_fmac_f32_e32 v120, v70, v30
	v_fmac_f32_e32 v120, v71, v31
	s_waitcnt lgkmcnt(11)
	v_fmac_f32_e32 v120, v72, v28
	v_fmac_f32_e32 v120, v73, v29
	v_fmac_f32_e32 v120, v74, v26
	v_fmac_f32_e32 v120, v75, v27
	s_waitcnt lgkmcnt(9)
	v_fmac_f32_e32 v120, v76, v24
	v_fmac_f32_e32 v120, v77, v25
	v_fmac_f32_e32 v120, v78, v22
	v_fmac_f32_e32 v120, v79, v23
	s_waitcnt lgkmcnt(7)
	v_fmac_f32_e32 v120, v80, v20
	v_fmac_f32_e32 v120, v81, v21
	v_fmac_f32_e32 v120, v82, v18
	v_fmac_f32_e32 v120, v83, v19
	s_waitcnt lgkmcnt(5)
	v_fmac_f32_e32 v120, v84, v16
	v_fmac_f32_e32 v120, v85, v17
	v_fmac_f32_e32 v120, v86, v14
	v_fmac_f32_e32 v120, v87, v15
	s_waitcnt lgkmcnt(3)
	v_fmac_f32_e32 v120, v88, v12
	v_fmac_f32_e32 v120, v89, v13
	v_fmac_f32_e32 v120, v90, v10
	v_fma_f32 v121, v60, v41, v55
	v_fmac_f32_e32 v121, v61, v38
	v_fmac_f32_e32 v121, v62, v39
	v_fmac_f32_e32 v121, v63, v36
	v_fmac_f32_e32 v121, v64, v37
	v_fmac_f32_e32 v121, v65, v34
	v_fmac_f32_e32 v121, v66, v35
	v_fmac_f32_e32 v121, v67, v32
	v_fmac_f32_e32 v121, v68, v33
	v_fmac_f32_e32 v121, v69, v30
	v_fmac_f32_e32 v121, v70, v31
	v_fmac_f32_e32 v121, v71, v28
	v_fmac_f32_e32 v121, v72, v29
	v_fmac_f32_e32 v121, v73, v26
	v_fmac_f32_e32 v121, v74, v27
	v_fmac_f32_e32 v121, v75, v24
	v_fmac_f32_e32 v121, v76, v25
	v_fmac_f32_e32 v121, v77, v22
	v_fmac_f32_e32 v121, v78, v23
	v_fmac_f32_e32 v121, v79, v20
	v_fmac_f32_e32 v121, v80, v21
	v_fmac_f32_e32 v121, v81, v18
	v_fmac_f32_e32 v121, v82, v19
	v_fmac_f32_e32 v121, v83, v16
	v_fmac_f32_e32 v121, v84, v17
	v_fmac_f32_e32 v121, v85, v14
	v_fmac_f32_e32 v121, v86, v15
	v_fmac_f32_e32 v121, v87, v12
	v_fmac_f32_e32 v121, v88, v13
	v_fmac_f32_e32 v121, v89, v10
	v_fmac_f32_e32 v121, v90, v11
	v_fma_f32 v122, v60, v38, v55
	v_fmac_f32_e32 v122, v61, v39
	v_fmac_f32_e32 v122, v62, v36
	v_fmac_f32_e32 v122, v63, v37
	v_fmac_f32_e32 v122, v64, v34
	v_fmac_f32_e32 v122, v65, v35
	v_fmac_f32_e32 v122, v66, v32
	v_fmac_f32_e32 v122, v67, v33
	v_fmac_f32_e32 v122, v68, v30
	v_fmac_f32_e32 v122, v69, v31
	v_fmac_f32_e32 v122, v70, v28
	v_fmac_f32_e32 v122, v71, v29
	v_fmac_f32_e32 v122, v72, v26
	v_fmac_f32_e32 v122, v73, v27
	v_fmac_f32_e32 v122, v74, v24
	v_fmac_f32_e32 v122, v75, v25
	v_fmac_f32_e32 v122, v76, v22
	v_fmac_f32_e32 v122, v77, v23
	v_fmac_f32_e32 v122, v78, v20
	v_fmac_f32_e32 v122, v79, v21
	v_fmac_f32_e32 v122, v80, v18
	v_fmac_f32_e32 v122, v81, v19
	v_fmac_f32_e32 v122, v82, v16
	v_fmac_f32_e32 v122, v83, v17
	v_fmac_f32_e32 v122, v84, v14
	v_fmac_f32_e32 v122, v85, v15
	v_fmac_f32_e32 v122, v86, v12
	v_fmac_f32_e32 v122, v87, v13
	v_fmac_f32_e32 v122, v88, v10
	v_fmac_f32_e32 v122, v89, v11
	s_waitcnt lgkmcnt(1)
	v_fmac_f32_e32 v122, v90, v8
	v_fma_f32 v123, v60, v39, v55
	v_fmac_f32_e32 v123, v61, v36
	v_fmac_f32_e32 v123, v62, v37
	v_fmac_f32_e32 v123, v63, v34
	v_fmac_f32_e32 v123, v64, v35
	v_fmac_f32_e32 v123, v65, v32
	v_fmac_f32_e32 v123, v66, v33
	v_fmac_f32_e32 v123, v67, v30
	v_fmac_f32_e32 v123, v68, v31
	v_fmac_f32_e32 v123, v69, v28
	v_fmac_f32_e32 v123, v70, v29
	v_fmac_f32_e32 v123, v71, v26
	v_fmac_f32_e32 v123, v72, v27
	v_fmac_f32_e32 v123, v73, v24
	v_fmac_f32_e32 v123, v74, v25
	v_fmac_f32_e32 v123, v75, v22
	v_fmac_f32_e32 v123, v76, v23
	v_fmac_f32_e32 v123, v77, v20
	v_fmac_f32_e32 v123, v78, v21
	v_fmac_f32_e32 v123, v79, v18
	v_fmac_f32_e32 v123, v80, v19
	v_fmac_f32_e32 v123, v81, v16
	v_fmac_f32_e32 v123, v82, v17
	v_fmac_f32_e32 v123, v83, v14
	v_fmac_f32_e32 v123, v84, v15
	v_fmac_f32_e32 v123, v85, v12
	v_fmac_f32_e32 v123, v86, v13
	v_fmac_f32_e32 v123, v87, v10
	v_fmac_f32_e32 v123, v88, v11
	v_fmac_f32_e32 v123, v89, v8
	v_fmac_f32_e32 v123, v90, v9
	v_fma_f32 v124, v60, v36, v55
	v_fmac_f32_e32 v124, v61, v37
	v_fmac_f32_e32 v124, v62, v34
	v_fmac_f32_e32 v124, v63, v35
	v_fmac_f32_e32 v124, v64, v32
	v_fmac_f32_e32 v124, v65, v33
	v_fmac_f32_e32 v124, v66, v30
	v_fmac_f32_e32 v124, v67, v31
	v_fmac_f32_e32 v124, v68, v28
	v_fmac_f32_e32 v124, v69, v29
	v_fmac_f32_e32 v124, v70, v26
	v_fmac_f32_e32 v124, v71, v27
	v_fmac_f32_e32 v124, v72, v24
	v_fmac_f32_e32 v124, v73, v25
	v_fmac_f32_e32 v124, v74, v22
	v_fmac_f32_e32 v124, v75, v23
	v_fmac_f32_e32 v124, v76, v20
; __device__ __forceinline__ void ph_conv2(const Params& p, int l, LAS unsigned char* lds, const int wvid) {
;     ...
;             for (int o = 0; o < 8; ++o) { float acc = cb;
; #pragma unroll
;                 for (int w = 0; w < 31; ++w) acc += wv[w] * x[o + w];
;                 const float mean = wave_sum(acc) * (1.f / 64.f); const float dv = acc - mean; const float var = wave_sum(dv * dv) * (1.f / 64.f);
	v_fmac_f32_e32 v124, v77, v21
	v_fmac_f32_e32 v124, v78, v18
	v_fmac_f32_e32 v124, v79, v19
	v_fmac_f32_e32 v124, v80, v16
	v_fmac_f32_e32 v124, v81, v17
	v_fmac_f32_e32 v124, v82, v14
	v_fmac_f32_e32 v124, v83, v15
	v_fmac_f32_e32 v124, v84, v12
	v_fmac_f32_e32 v124, v85, v13
	v_fmac_f32_e32 v124, v86, v10
	v_fmac_f32_e32 v124, v87, v11
	v_fmac_f32_e32 v124, v88, v8
	v_fmac_f32_e32 v124, v89, v9
	v_fmac_f32_e32 v124, v90, v6
	v_fma_f32 v125, v60, v37, v55
	v_fmac_f32_e32 v125, v61, v34
	v_fmac_f32_e32 v125, v62, v35
	v_fmac_f32_e32 v125, v63, v32
	v_fmac_f32_e32 v125, v64, v33
	v_fmac_f32_e32 v125, v65, v30
	v_fmac_f32_e32 v125, v66, v31
	v_fmac_f32_e32 v125, v67, v28
	v_fmac_f32_e32 v125, v68, v29
	v_fmac_f32_e32 v125, v69, v26
	v_fmac_f32_e32 v125, v70, v27
	v_fmac_f32_e32 v125, v71, v24
	v_fmac_f32_e32 v125, v72, v25
	v_fmac_f32_e32 v125, v73, v22
	v_fmac_f32_e32 v125, v74, v23
	v_fmac_f32_e32 v125, v75, v20
	v_fmac_f32_e32 v125, v76, v21
	v_fmac_f32_e32 v125, v77, v18
	v_fmac_f32_e32 v125, v78, v19
	v_fmac_f32_e32 v125, v79, v16
	v_fmac_f32_e32 v125, v80, v17
	v_fmac_f32_e32 v125, v81, v14
	v_fmac_f32_e32 v125, v82, v15
	v_fmac_f32_e32 v125, v83, v12
	v_fmac_f32_e32 v125, v84, v13
	v_fmac_f32_e32 v125, v85, v10
	v_fmac_f32_e32 v125, v86, v11
	v_fmac_f32_e32 v125, v87, v8
	v_fmac_f32_e32 v125, v88, v9
	v_fmac_f32_e32 v125, v89, v6
	v_fmac_f32_e32 v125, v90, v7
	v_fma_f32 v126, v60, v34, v55
	v_fmac_f32_e32 v126, v61, v35
	v_fmac_f32_e32 v126, v62, v32
	v_fmac_f32_e32 v126, v63, v33
	v_fmac_f32_e32 v126, v64, v30
	v_fmac_f32_e32 v126, v65, v31
	v_fmac_f32_e32 v126, v66, v28
	v_fmac_f32_e32 v126, v67, v29
	v_fmac_f32_e32 v126, v68, v26
	v_fmac_f32_e32 v126, v69, v27
	v_fmac_f32_e32 v126, v70, v24
	v_fmac_f32_e32 v126, v71, v25
	v_fmac_f32_e32 v126, v72, v22
	v_fmac_f32_e32 v126, v73, v23
	v_fmac_f32_e32 v126, v74, v20
	v_fmac_f32_e32 v126, v75, v21
	v_fmac_f32_e32 v126, v76, v18
	v_fmac_f32_e32 v126, v77, v19
	v_fmac_f32_e32 v126, v78, v16
	v_fmac_f32_e32 v126, v79, v17
	v_fmac_f32_e32 v126, v80, v14
	v_fmac_f32_e32 v126, v81, v15
	v_fmac_f32_e32 v126, v82, v12
	v_fmac_f32_e32 v126, v83, v13
	v_fmac_f32_e32 v126, v84, v10
	v_fmac_f32_e32 v126, v85, v11
	v_fmac_f32_e32 v126, v86, v8
	v_fmac_f32_e32 v126, v87, v9
	v_fmac_f32_e32 v126, v88, v6
	v_fmac_f32_e32 v126, v89, v7
	s_waitcnt lgkmcnt(0)
	v_fmac_f32_e32 v126, v90, v4
	v_fma_f32 v127, v60, v35, v55
	v_fmac_f32_e32 v127, v61, v32
	v_fmac_f32_e32 v127, v62, v33
	v_fmac_f32_e32 v127, v63, v30
	v_fmac_f32_e32 v127, v64, v31
	v_fmac_f32_e32 v127, v65, v28
	v_fmac_f32_e32 v127, v66, v29
	v_fmac_f32_e32 v127, v67, v26
	v_fmac_f32_e32 v127, v68, v27
	v_fmac_f32_e32 v127, v69, v24
	v_fmac_f32_e32 v127, v70, v25
	v_fmac_f32_e32 v127, v71, v22
	v_fmac_f32_e32 v127, v72, v23
	v_fmac_f32_e32 v127, v73, v20
	v_fmac_f32_e32 v127, v74, v21
	v_fmac_f32_e32 v127, v75, v18
	v_fmac_f32_e32 v127, v76, v19
	v_fmac_f32_e32 v127, v77, v16
	v_fmac_f32_e32 v127, v78, v17
	v_fmac_f32_e32 v127, v79, v14
	v_fmac_f32_e32 v127, v80, v15
	v_fmac_f32_e32 v127, v81, v12
	v_fmac_f32_e32 v127, v82, v13
	v_fmac_f32_e32 v127, v83, v10
	v_fmac_f32_e32 v127, v84, v11
	v_fmac_f32_e32 v127, v85, v8
	v_fmac_f32_e32 v127, v86, v9
	v_fmac_f32_e32 v127, v87, v6
	v_fmac_f32_e32 v127, v88, v7
	v_fmac_f32_e32 v127, v89, v4
	v_fmac_f32_e32 v127, v90, v5
	s_mov_b32 vcc_lo, 0x5a5a5a5a
	s_mov_b32 vcc_hi, 0x5a5a5a5a
	v_cndmask_b32_e32 v136, v121, v120, vcc
	v_cndmask_b32_e32 v137, v123, v122, vcc
	v_cndmask_b32_e32 v138, v125, v124, vcc
	v_cndmask_b32_e32 v139, v127, v126, vcc
	v_cndmask_b32_e32 v140, v120, v121, vcc
	v_cndmask_b32_e32 v141, v122, v123, vcc
	v_cndmask_b32_e32 v142, v124, v125, vcc
	v_cndmask_b32_e32 v143, v126, v127, vcc
	v_add_f32_dpp v144, v136, v140 quad_perm:[1,0,3,2] row_mask:0xf bank_mask:0xf
	v_add_f32_dpp v145, v137, v141 quad_perm:[1,0,3,2] row_mask:0xf bank_mask:0xf
	v_add_f32_dpp v146, v138, v142 quad_perm:[1,0,3,2] row_mask:0xf bank_mask:0xf
	v_add_f32_dpp v147, v139, v143 quad_perm:[1,0,3,2] row_mask:0xf bank_mask:0xf
	s_mov_b32 vcc_lo, 0x3c3c3c3c
	s_mov_b32 vcc_hi, 0x3c3c3c3c
	v_cndmask_b32_e32 v148, v145, v144, vcc
	v_cndmask_b32_e32 v149, v147, v146, vcc
	v_cndmask_b32_e32 v150, v144, v145, vcc
	v_cndmask_b32_e32 v151, v146, v147, vcc
	s_nop 0
	v_add_f32_dpp v136, v148, v150 quad_perm:[2,3,0,1] row_mask:0xf bank_mask:0xf
	v_add_f32_dpp v137, v149, v151 quad_perm:[2,3,0,1] row_mask:0xf bank_mask:0xf
	s_mov_b32 vcc_lo, 0xff00ff00
	s_mov_b32 vcc_hi, 0xff00ff00
	v_cndmask_b32_e32 v138, v137, v136, vcc
	v_cndmask_b32_e32 v139, v136, v137, vcc
	s_nop 1
	v_add_f32_dpp v140, v138, v139 row_ror:8 row_mask:0xf bank_mask:0xf
	s_nop 1
	v_add_f32_dpp v141, v140, v140 row_half_mirror row_mask:0xf bank_mask:0xf
	v_mov_b32_e32 v142, v141
	s_nop 1
	v_permlane16_swap_b32_e32 v141, v142
	v_add_f32_e32 v143, v141, v142
	v_mov_b32_e32 v144, v143
	s_nop 1
	v_permlane32_swap_b32_e32 v143, v144
	v_add_f32_e32 v145, v143, v144
	s_nop 0
	v_readlane_b32 s24, v145, 0
; __device__ __forceinline__ bf16_t f2bf(float f) { unsigned u = __float_as_uint(f); u += 0x7FFFu + ((u >> 16) & 1u); return (bf16_t)(u >> 16); }
; __device__ __forceinline__ float frsq(float x) { return __builtin_amdgcn_rsqf(x); }
; __device__ __forceinline__ float sigmoidf_(float x) { return frcp(1.0f + __expf(-x)); }
; __device__ __forceinline__ void ph_conv2(const Params& p, int l, LAS unsigned char* lds, const int wvid) {
;     ...
;                 const float mean = wave_sum(acc) * (1.f / 64.f); const float dv = acc - mean; const float var = wave_sum(dv * dv) * (1.f / 64.f);
;                 const float y = dv * frsq(var + 1e-5f) * gg + gb;
;                 const int tg = t0 + tl + o;
;                 if (tg < LT) MIX[((size_t)b * LT + tg) * D + M_D + c] = f2bf(y * sigmoidf_(y)); }
	v_readlane_b32 s25, v145, 1
	v_readlane_b32 s26, v145, 2
	v_readlane_b32 s27, v145, 3
	v_readlane_b32 s28, v145, 8
	v_readlane_b32 s29, v145, 9
	v_readlane_b32 s30, v145, 10
	v_readlane_b32 s31, v145, 11
	v_fmac_f32_e32 v120, s24, v214
	v_fmac_f32_e32 v121, s25, v214
	v_fmac_f32_e32 v122, s26, v214
	v_fmac_f32_e32 v123, s27, v214
	v_fmac_f32_e32 v124, s28, v214
	v_fmac_f32_e32 v125, s29, v214
	v_fmac_f32_e32 v126, s30, v214
	v_fmac_f32_e32 v127, s31, v214
	v_mul_f32_e32 v128, v120, v120
	v_mul_f32_e32 v129, v121, v121
	v_mul_f32_e32 v130, v122, v122
	v_mul_f32_e32 v131, v123, v123
	v_mul_f32_e32 v132, v124, v124
	v_mul_f32_e32 v133, v125, v125
	v_mul_f32_e32 v134, v126, v126
	v_mul_f32_e32 v135, v127, v127
	s_mov_b32 vcc_lo, 0x5a5a5a5a
	s_mov_b32 vcc_hi, 0x5a5a5a5a
	v_cndmask_b32_e32 v136, v129, v128, vcc
	v_cndmask_b32_e32 v137, v131, v130, vcc
	v_cndmask_b32_e32 v138, v133, v132, vcc
	v_cndmask_b32_e32 v139, v135, v134, vcc
	v_cndmask_b32_e32 v140, v128, v129, vcc
	v_cndmask_b32_e32 v141, v130, v131, vcc
	v_cndmask_b32_e32 v142, v132, v133, vcc
	v_cndmask_b32_e32 v143, v134, v135, vcc
	v_add_f32_dpp v144, v136, v140 quad_perm:[1,0,3,2] row_mask:0xf bank_mask:0xf
	v_add_f32_dpp v145, v137, v141 quad_perm:[1,0,3,2] row_mask:0xf bank_mask:0xf
	v_add_f32_dpp v146, v138, v142 quad_perm:[1,0,3,2] row_mask:0xf bank_mask:0xf
	v_add_f32_dpp v147, v139, v143 quad_perm:[1,0,3,2] row_mask:0xf bank_mask:0xf
	s_mov_b32 vcc_lo, 0x3c3c3c3c
	s_mov_b32 vcc_hi, 0x3c3c3c3c
	v_cndmask_b32_e32 v148, v145, v144, vcc
	v_cndmask_b32_e32 v149, v147, v146, vcc
	v_cndmask_b32_e32 v150, v144, v145, vcc
	v_cndmask_b32_e32 v151, v146, v147, vcc
	s_nop 0
	v_add_f32_dpp v136, v148, v150 quad_perm:[2,3,0,1] row_mask:0xf bank_mask:0xf
	v_add_f32_dpp v137, v149, v151 quad_perm:[2,3,0,1] row_mask:0xf bank_mask:0xf
	s_mov_b32 vcc_lo, 0xff00ff00
	s_mov_b32 vcc_hi, 0xff00ff00
	v_cndmask_b32_e32 v138, v137, v136, vcc
	v_cndmask_b32_e32 v139, v136, v137, vcc
	s_nop 1
	v_add_f32_dpp v140, v138, v139 row_ror:8 row_mask:0xf bank_mask:0xf
	s_nop 1
	v_add_f32_dpp v141, v140, v140 row_half_mirror row_mask:0xf bank_mask:0xf
	v_mov_b32_e32 v142, v141
	s_nop 1
	v_permlane16_swap_b32_e32 v141, v142
	v_add_f32_e32 v143, v141, v142
	v_mov_b32_e32 v144, v143
	s_nop 1
	v_permlane32_swap_b32_e32 v143, v144
	v_add_f32_e32 v145, v143, v144
	v_fma_f32 v145, v145, v215, v204
	v_rsq_f32_e32 v145, v145
	s_nop 0
	v_readlane_b32 s24, v145, 0
	v_readlane_b32 s25, v145, 1
	v_readlane_b32 s26, v145, 2
	v_readlane_b32 s27, v145, 3
	v_readlane_b32 s28, v145, 8
	v_readlane_b32 s29, v145, 9
	v_readlane_b32 s30, v145, 10
	v_readlane_b32 s31, v145, 11
	v_mul_f32_e32 v120, s24, v120
	v_mul_f32_e32 v121, s25, v121
	v_mul_f32_e32 v122, s26, v122
	v_mul_f32_e32 v123, s27, v123
	v_mul_f32_e32 v124, s28, v124
	v_mul_f32_e32 v125, s29, v125
	v_mul_f32_e32 v126, s30, v126
	v_mul_f32_e32 v127, s31, v127
	v_fma_f32 v120, v58, v120, v59
	v_fma_f32 v121, v58, v121, v59
	v_fma_f32 v122, v58, v122, v59
	v_fma_f32 v123, v58, v123, v59
	v_fma_f32 v124, v58, v124, v59
	v_fma_f32 v125, v58, v125, v59
	v_fma_f32 v126, v58, v126, v59
	v_fma_f32 v127, v58, v127, v59
	v_mul_f32_e32 v128, 0xbfb8aa3b, v120
	v_mul_f32_e32 v129, 0xbfb8aa3b, v121
	v_mul_f32_e32 v130, 0xbfb8aa3b, v122
	v_mul_f32_e32 v131, 0xbfb8aa3b, v123
	v_mul_f32_e32 v132, 0xbfb8aa3b, v124
	v_mul_f32_e32 v133, 0xbfb8aa3b, v125
	v_mul_f32_e32 v134, 0xbfb8aa3b, v126
	v_mul_f32_e32 v135, 0xbfb8aa3b, v127
	v_exp_f32_e32 v128, v128
	v_exp_f32_e32 v129, v129
	v_exp_f32_e32 v130, v130
	v_exp_f32_e32 v131, v131
	v_exp_f32_e32 v132, v132
	v_exp_f32_e32 v133, v133
	v_exp_f32_e32 v134, v134
	v_exp_f32_e32 v135, v135
	v_add_f32_e32 v128, 1.0, v128
	v_add_f32_e32 v129, 1.0, v129
	v_add_f32_e32 v130, 1.0, v130
	v_add_f32_e32 v131, 1.0, v131
	v_add_f32_e32 v132, 1.0, v132
	v_add_f32_e32 v133, 1.0, v133
	v_add_f32_e32 v134, 1.0, v134
	v_add_f32_e32 v135, 1.0, v135
	v_rcp_f32_e32 v128, v128
	v_rcp_f32_e32 v129, v129
	v_rcp_f32_e32 v130, v130
	v_rcp_f32_e32 v131, v131
	v_rcp_f32_e32 v132, v132
	v_rcp_f32_e32 v133, v133
	v_rcp_f32_e32 v134, v134
	v_rcp_f32_e32 v135, v135
	v_mul_f32_e32 v120, v120, v128
	v_mul_f32_e32 v121, v121, v129
	v_mul_f32_e32 v122, v122, v130
	v_mul_f32_e32 v123, v123, v131
	v_mul_f32_e32 v124, v124, v132
	v_mul_f32_e32 v125, v125, v133
	v_mul_f32_e32 v126, v126, v134
	v_mul_f32_e32 v127, v127, v135
	v_cvt_pk_bf16_f32 v120, v120, v120
	v_cvt_pk_bf16_f32 v121, v121, v121
	v_cvt_pk_bf16_f32 v122, v122, v122
	v_cvt_pk_bf16_f32 v123, v123, v123
	v_cvt_pk_bf16_f32 v124, v124, v124
	v_cvt_pk_bf16_f32 v125, v125, v125
	v_cvt_pk_bf16_f32 v126, v126, v126
	v_cvt_pk_bf16_f32 v127, v127, v127
	v_readfirstlane_b32 s26, v2
	s_mov_b64 s[28:29], 0x1000
	v_mov_b32_e32 v4, v2
	v_ashrrev_i32_e32 v5, 31, v4
	v_lshl_add_u64 v[4:5], s[6:7], 0, v[4:5]
	v_lshlrev_b64 v[4:5], 11, v[4:5]
	v_lshl_add_u64 v[4:5], v[56:57], 0, v[4:5]
	s_add_i32 s27, s26, 0
	s_cmp_lt_i32 s27, s33
	s_cbranch_scc0 .Lcv_st0
	global_store_short v[4:5], v120, off
